# scan store ladder: alternate two temp register pairs between consecutive stores (breaks reuse serialization); on top of v130
# speedup vs baseline: 1.0112x; 1.0036x over previous
; #define LAS __attribute__((address_space(3)))
; __device__ __forceinline__ float bf_lo(unsigned w) { return __uint_as_float(w << 16); }
; __device__ __forceinline__ float bf_hi(unsigned w) { return __uint_as_float(w & 0xffff0000u); }
; #define MFMA32(a, b, c) __builtin_amdgcn_mfma_f32_32x32x16_bf16((a), (b), (c), 0, 0, 0)
; __device__ __forceinline__ bf16x8 pack_step(const f32x16& x, int s) { return __builtin_bit_cast(bf16x8, ((u32x4){pk(x[8 * s], x[8 * s + 1]), pk(x[8 * s + 2], x[8 * s + 3]), pk(x[8 * s + 4], x[8 * s + 5]), pk(x[8 * s + 6], x[8 * s + 7])})); }
; __device__ __forceinline__ void p4_scan(Frame& F) {
;     ...
;         const LAS unsigned char* lb = F.lds + (n & 1) * UNIT_DMA;
;         const float dlc = *(const LAS float*)(lb + UO_DL);
;         u32x4 ucur[2][2];
; #pragma unroll
;         for (int mt = 0; mt < 2; ++mt) { ucur[mt][0] = *(const LAS u32x4*)(lb + UO_U + (mt * 4 + nt) * 2048 + lane * 32); ucur[mt][1] = *(const LAS u32x4*)(lb + UO_U + (mt * 4 + nt) * 2048 + lane * 32 + 16); }
;     ...
;         f32x16 VN[2], O[2];
; #pragma unroll
;         for (int mt = 0; mt < 2; ++mt) {
; #pragma unroll
;             for (int p = 0; p < 4; ++p) { VN[mt][2 * p] = bf_lo(ucur[mt][0][p]); VN[mt][2 * p + 1] = bf_hi(ucur[mt][0][p]); VN[mt][8 + 2 * p] = bf_lo(ucur[mt][1][p]); VN[mt][8 + 2 * p + 1] = bf_hi(ucur[mt][1][p]); }
; #pragma unroll
;             for (int i = 0; i < 16; ++i) O[mt][i] = 0.f; }
; #pragma unroll
;         for (int kt = 0; kt < 4; ++kt) { const bf16x8 sb0 = pack_step(S[kt], 0), sb1 = pack_step(S[kt], 1);
; #pragma unroll
;             for (int mt = 0; mt < 2; ++mt) { const int fi = (mt * 4 + kt) * 2;
;                 VN[mt] = MFMA32(FRAG(UO_NW, fi), sb0, VN[mt]); VN[mt] = MFMA32(FRAG(UO_NW, fi + 1), sb1, VN[mt]);
;                 O[mt] = MFMA32(FRAG(UO_QD, fi), sb0, O[mt]); O[mt] = MFMA32(FRAG(UO_QD, fi + 1), sb1, O[mt]); } }
.LBB0_641:
	s_bitcmp1_b32 s64, 0
	s_cselect_b32 s48, 0x12400, 0
	s_add_i32 s48, s48, 0
	s_add_i32 s49, s48, s60
	v_add_u32_e32 v66, s49, v1
	v_add_u32_e32 v177, s48, v140
	ds_read_b128 v[70:73], v66 offset:57344
	v_add_u32_e32 v67, 0xe000, v66
	ds_read_b128 v[78:81], v66 offset:57360
	ds_read_b128 v[86:89], v67 offset:8192
	ds_read_b128 v[82:85], v67 offset:8208
	ds_read_b128 v[94:97], v177
	v_cvt_pk_bf16_f32 v90, v2, v3
	s_waitcnt lgkmcnt(0)
	v_lshlrev_b32_e32 v66, 16, v70
	v_and_b32_e32 v67, 0xffff0000, v70
	v_lshlrev_b32_e32 v74, 16, v78
	v_and_b32_e32 v75, 0xffff0000, v78
	v_lshlrev_b32_e32 v68, 16, v71
	v_and_b32_e32 v69, 0xffff0000, v71
	v_lshlrev_b32_e32 v76, 16, v79
	v_and_b32_e32 v77, 0xffff0000, v79
	v_lshlrev_b32_e32 v70, 16, v72
	v_and_b32_e32 v71, 0xffff0000, v72
	v_lshlrev_b32_e32 v78, 16, v80
	v_and_b32_e32 v79, 0xffff0000, v80
	v_lshlrev_b32_e32 v72, 16, v73
	v_and_b32_e32 v73, 0xffff0000, v73
	v_lshlrev_b32_e32 v80, 16, v81
	v_and_b32_e32 v81, 0xffff0000, v81
	v_cvt_pk_bf16_f32 v91, v4, v5
	v_cvt_pk_bf16_f32 v92, v6, v7
	v_cvt_pk_bf16_f32 v93, v8, v9
	ds_read_b128 v[98:101], v177 offset:1024
	ds_read_b128 v[130:133], v177 offset:56320
	v_mfma_f32_32x32x16_bf16 v[66:81], v[94:97], v[90:93], v[66:81]
	ds_read_b128 v[94:97], v177 offset:16384
	ds_read_b128 v[182:185], v177 offset:2048
	v_cvt_pk_bf16_f32 v178, v10, v11
	v_cvt_pk_bf16_f32 v179, v12, v13
	v_cvt_pk_bf16_f32 v180, v14, v15
	v_cvt_pk_bf16_f32 v181, v16, v17
	ds_read_b128 v[134:137], v177 offset:32768
	ds_read_b128 v[126:129], v177 offset:17408
	ds_read_b128 v[186:189], v177 offset:15360
	s_waitcnt lgkmcnt(0)
	v_mfma_f32_32x32x16_bf16 v[66:81], v[98:101], v[178:181], v[66:81]
	v_lshlrev_b32_e32 v114, 16, v86
	v_and_b32_e32 v115, 0xffff0000, v86
	v_lshlrev_b32_e32 v122, 16, v82
	v_and_b32_e32 v123, 0xffff0000, v82
	v_lshlrev_b32_e32 v116, 16, v87
	v_and_b32_e32 v117, 0xffff0000, v87
	v_lshlrev_b32_e32 v124, 16, v83
	v_mfma_f32_32x32x16_bf16 v[98:113], v[94:97], v[90:93], 0
	ds_read_b128 v[94:97], v177 offset:8192
	ds_read_b128 v[190:193], v177 offset:18432
	v_and_b32_e32 v125, 0xffff0000, v83
	v_lshlrev_b32_e32 v118, 16, v88
	v_and_b32_e32 v119, 0xffff0000, v88
	v_lshlrev_b32_e32 v120, 16, v89
	v_and_b32_e32 v121, 0xffff0000, v89
	ds_read_b128 v[194:197], v177 offset:7168
	v_mfma_f32_32x32x16_bf16 v[98:113], v[126:129], v[178:181], v[98:113]
	v_lshlrev_b32_e32 v126, 16, v84
	v_and_b32_e32 v127, 0xffff0000, v84
	v_lshlrev_b32_e32 v128, 16, v85
	v_and_b32_e32 v129, 0xffff0000, v85
	ds_read_b128 v[82:85], v177 offset:9216
	ds_read_b128 v[198:201], v177 offset:10240
	s_add_i32 s48, s48, 0x12000
	s_cmp_gt_u32 s64, 3
	s_waitcnt lgkmcnt(0)
	v_mfma_f32_32x32x16_bf16 v[114:129], v[94:97], v[90:93], v[114:129]
	v_mfma_f32_32x32x16_bf16 v[114:129], v[82:85], v[178:181], v[114:129]
	ds_read_b128 v[82:85], v177 offset:24576
	ds_read_b128 v[202:205], v177 offset:23552
	ds_read_b128 v[206:209], v177 offset:25600
	ds_read_b128 v[210:213], v177 offset:26624
	ds_read_b128 v[214:217], v177 offset:4096
	s_waitcnt lgkmcnt(0)
	v_mfma_f32_32x32x16_bf16 v[82:97], v[82:85], v[90:93], 0
	v_mfma_f32_32x32x16_bf16 v[82:97], v[206:209], v[178:181], v[82:97]
	v_cvt_pk_bf16_f32 v178, v18, v19
	v_cvt_pk_bf16_f32 v179, v20, v21
	v_cvt_pk_bf16_f32 v180, v22, v23
	v_cvt_pk_bf16_f32 v181, v24, v25
	v_cvt_pk_bf16_f32 v206, v26, v27
	v_cvt_pk_bf16_f32 v207, v28, v29
	v_cvt_pk_bf16_f32 v208, v30, v31
	v_mfma_f32_32x32x16_bf16 v[66:81], v[182:185], v[178:181], v[66:81]
	ds_read_b128 v[182:185], v177 offset:3072
	v_cvt_pk_bf16_f32 v209, v32, v33
	v_mfma_f32_32x32x16_bf16 v[98:113], v[190:193], v[178:181], v[98:113]
	s_waitcnt lgkmcnt(0)
	v_mfma_f32_32x32x16_bf16 v[66:81], v[182:185], v[206:209], v[66:81]
	ds_read_b128 v[182:185], v177 offset:19456
	ds_read_b128 v[190:193], v177 offset:20480
	v_mfma_f32_32x32x16_bf16 v[114:129], v[198:201], v[178:181], v[114:129]
	s_waitcnt lgkmcnt(0)
	v_mfma_f32_32x32x16_bf16 v[98:113], v[182:185], v[206:209], v[98:113]
	ds_read_b128 v[182:185], v177 offset:11264
	ds_read_b128 v[198:201], v177 offset:12288
	v_mfma_f32_32x32x16_bf16 v[82:97], v[210:213], v[178:181], v[82:97]
	v_cvt_pk_bf16_f32 v210, v42, v43
	v_cvt_pk_bf16_f32 v211, v44, v45
	v_cvt_pk_bf16_f32 v212, v46, v47
	v_cvt_pk_bf16_f32 v213, v48, v49
	s_waitcnt lgkmcnt(0)
	v_mfma_f32_32x32x16_bf16 v[114:129], v[182:185], v[206:209], v[114:129]
	ds_read_b128 v[178:181], v177 offset:27648
	ds_read_b128 v[182:185], v177 offset:28672
	s_waitcnt lgkmcnt(0)
	v_mfma_f32_32x32x16_bf16 v[82:97], v[178:181], v[206:209], v[82:97]
	v_cvt_pk_bf16_f32 v178, v34, v35
	v_cvt_pk_bf16_f32 v179, v36, v37
	v_cvt_pk_bf16_f32 v180, v38, v39
	v_cvt_pk_bf16_f32 v181, v40, v41
	ds_read_b128 v[206:209], v177 offset:5120
	s_nop 0
	v_mfma_f32_32x32x16_bf16 v[66:81], v[214:217], v[178:181], v[66:81]
	ds_read_b128 v[214:217], v177 offset:6144
	v_mfma_f32_32x32x16_bf16 v[98:113], v[190:193], v[178:181], v[98:113]
	s_waitcnt lgkmcnt(0)
	v_mfma_f32_32x32x16_bf16 v[66:81], v[206:209], v[210:213], v[66:81]
	ds_read_b128 v[190:193], v177 offset:21504
	ds_read_b128 v[206:209], v177 offset:22528
	v_mfma_f32_32x32x16_bf16 v[114:129], v[198:201], v[178:181], v[114:129]
	v_mfma_f32_32x32x16_bf16 v[82:97], v[182:185], v[178:181], v[82:97]
	s_waitcnt lgkmcnt(0)
	v_mfma_f32_32x32x16_bf16 v[98:113], v[190:193], v[210:213], v[98:113]
	ds_read_b128 v[190:193], v177 offset:13312
	ds_read_b128 v[198:201], v177 offset:14336
	ds_read_b128 v[178:181], v177 offset:29696
	ds_read_b128 v[182:185], v177 offset:30720
	s_waitcnt lgkmcnt(0)
; #define MFMA32(a, b, c) __builtin_amdgcn_mfma_f32_32x32x16_bf16((a), (b), (c), 0, 0, 0)
; __device__ __forceinline__ bf16x8 pack_step(const f32x16& x, int s) { return __builtin_bit_cast(bf16x8, ((u32x4){pk(x[8 * s], x[8 * s + 1]), pk(x[8 * s + 2], x[8 * s + 3]), pk(x[8 * s + 4], x[8 * s + 5]), pk(x[8 * s + 6], x[8 * s + 7])})); }
; __device__ __forceinline__ void p4_scan(Frame& F) {
;     ...
;         bf16x8 vb[2][2];
; #pragma unroll
;         for (int ct = 0; ct < 2; ++ct) { vb[ct][0] = pack_step(VN[ct], 0); vb[ct][1] = pack_step(VN[ct], 1); }
; #pragma unroll
;         for (int mt = 0; mt < 2; ++mt)
; #pragma unroll
;             for (int ct = 0; ct < 2; ++ct) { const int fi = (mt * 2 + ct) * 2; O[mt] = MFMA32(FRAG(UO_QK, fi), vb[ct][0], O[mt]); O[mt] = MFMA32(FRAG(UO_QK, fi + 1), vb[ct][1], O[mt]); }
; #pragma unroll
;         for (int kt = 0; kt < 4; ++kt) {
; #pragma unroll
;             for (int i = 0; i < 16; ++i) S[kt][i] *= dlc;
; #pragma unroll
;             for (int ct = 0; ct < 2; ++ct) { const int fi = (kt * 2 + ct) * 2; S[kt] = MFMA32(FRAG(UO_KDT, fi), vb[ct][0], S[kt]); S[kt] = MFMA32(FRAG(UO_KDT, fi + 1), vb[ct][1], S[kt]); } }
;     ...
;         const int cidx = STEP_CIDX(n);
;         stored = cidx >= CTXL / 64;
	v_mfma_f32_32x32x16_bf16 v[114:129], v[190:193], v[210:213], v[114:129]
	v_cvt_pk_bf16_f32 v190, v58, v59
	v_cvt_pk_bf16_f32 v191, v60, v61
	v_cvt_pk_bf16_f32 v192, v62, v63
	v_cvt_pk_bf16_f32 v193, v64, v65
	v_mfma_f32_32x32x16_bf16 v[82:97], v[178:181], v[210:213], v[82:97]
	v_cvt_pk_bf16_f32 v178, v50, v51
	v_cvt_pk_bf16_f32 v179, v52, v53
	v_cvt_pk_bf16_f32 v180, v54, v55
	v_cvt_pk_bf16_f32 v181, v56, v57
	s_nop 1
	v_mfma_f32_32x32x16_bf16 v[66:81], v[214:217], v[178:181], v[66:81]
	v_mfma_f32_32x32x16_bf16 v[98:113], v[206:209], v[178:181], v[98:113]
	v_mfma_f32_32x32x16_bf16 v[114:129], v[198:201], v[178:181], v[114:129]
	v_mfma_f32_32x32x16_bf16 v[82:97], v[182:185], v[178:181], v[82:97]
	ds_read_b128 v[178:181], v177 offset:31744
	v_mfma_f32_32x32x16_bf16 v[66:81], v[194:197], v[190:193], v[66:81]
	s_waitcnt lgkmcnt(0)
	v_mfma_f32_32x32x16_bf16 v[82:97], v[178:181], v[190:193], v[82:97]
	ds_read_b128 v[178:181], v177 offset:49152
	s_nop 8
	v_cvt_pk_bf16_f32 v66, v66, v67
	v_cvt_pk_bf16_f32 v67, v68, v69
	v_cvt_pk_bf16_f32 v68, v70, v71
	v_cvt_pk_bf16_f32 v69, v72, v73
	ds_read_b128 v[70:73], v177 offset:48128
	v_cvt_pk_bf16_f32 v74, v74, v75
	v_mfma_f32_32x32x16_bf16 v[98:113], v[202:205], v[190:193], v[98:113]
	v_cvt_pk_bf16_f32 v75, v76, v77
	v_cvt_pk_bf16_f32 v76, v78, v79
	v_cvt_pk_bf16_f32 v77, v80, v81
	ds_read_b128 v[78:81], v177 offset:51200
	s_waitcnt lgkmcnt(0)
	v_mfma_f32_32x32x16_bf16 v[98:113], v[178:181], v[66:69], v[98:113]
	ds_read_b128 v[178:181], v177 offset:50176
	v_mfma_f32_32x32x16_bf16 v[114:129], v[186:189], v[190:193], v[114:129]
	s_waitcnt lgkmcnt(0)
	v_mfma_f32_32x32x16_bf16 v[98:113], v[178:181], v[74:77], v[98:113]
	s_nop 9
	v_cvt_pk_bf16_f32 v114, v114, v115
	v_cvt_pk_bf16_f32 v115, v116, v117
	v_cvt_pk_bf16_f32 v116, v118, v119
	v_cvt_pk_bf16_f32 v117, v120, v121
	v_cvt_pk_bf16_f32 v118, v122, v123
	v_cvt_pk_bf16_f32 v119, v124, v125
	ds_read_b128 v[122:125], v177 offset:53248
	v_mfma_f32_32x32x16_bf16 v[98:113], v[78:81], v[114:117], v[98:113]
	ds_read_b128 v[78:81], v177 offset:52224
	v_cvt_pk_bf16_f32 v120, v126, v127
	v_cvt_pk_bf16_f32 v121, v128, v129
	s_waitcnt lgkmcnt(0)
	v_mfma_f32_32x32x16_bf16 v[82:97], v[122:125], v[66:69], v[82:97]
	v_mfma_f32_32x32x16_bf16 v[98:113], v[78:81], v[118:121], v[98:113]
	ds_read_b128 v[78:81], v177 offset:54272
	ds_read_b128 v[122:125], v177 offset:55296
	s_waitcnt lgkmcnt(0)
	v_mfma_f32_32x32x16_bf16 v[82:97], v[78:81], v[74:77], v[82:97]
	v_mov_b32_e32 v78, s48
	ds_read_b32 v126, v78
	s_cselect_b32 s48, 0x87, 3
	s_add_i32 s48, s48, s62
	s_add_i32 s65, s48, 0xffffff7a
	s_and_b64 s[48:49], s[0:1], exec
	s_waitcnt lgkmcnt(0)
	v_pk_mul_f32 v[16:17], v[16:17], v[126:127] op_sel_hi:[1,0]
	v_pk_mul_f32 v[14:15], v[14:15], v[126:127] op_sel_hi:[1,0]
	v_pk_mul_f32 v[12:13], v[12:13], v[126:127] op_sel_hi:[1,0]
	v_pk_mul_f32 v[10:11], v[10:11], v[126:127] op_sel_hi:[1,0]
	v_pk_mul_f32 v[8:9], v[8:9], v[126:127] op_sel_hi:[1,0]
	v_pk_mul_f32 v[6:7], v[6:7], v[126:127] op_sel_hi:[1,0]
	v_pk_mul_f32 v[4:5], v[4:5], v[126:127] op_sel_hi:[1,0]
	v_pk_mul_f32 v[2:3], v[2:3], v[126:127] op_sel_hi:[1,0]
	v_mfma_f32_32x32x16_bf16 v[82:97], v[122:125], v[114:117], v[82:97]
	ds_read_b128 v[78:81], v177 offset:33792
	ds_read_b128 v[122:125], v177 offset:34816
	v_mul_f32_e64 v32, v32, v126
	v_mul_f32_e64 v33, v33, v126
	v_mul_f32_e64 v30, v30, v126
	v_mul_f32_e64 v31, v31, v126
	v_pk_mul_f32 v[28:29], v[28:29], v[126:127] op_sel_hi:[1,0]
	v_pk_mul_f32 v[26:27], v[26:27], v[126:127] op_sel_hi:[1,0]
	v_pk_mul_f32 v[24:25], v[24:25], v[126:127] op_sel_hi:[1,0]
	v_pk_mul_f32 v[22:23], v[22:23], v[126:127] op_sel_hi:[1,0]
	v_mfma_f32_32x32x16_bf16 v[2:17], v[134:137], v[66:69], v[2:17]
	v_mul_f32_e64 v20, v20, v126
	v_mul_f32_e64 v21, v21, v126
	v_mul_f32_e64 v18, v18, v126
	v_mul_f32_e64 v19, v19, v126
	v_mul_f32_e64 v48, v48, v126
	v_mul_f32_e64 v49, v49, v126
	v_pk_mul_f32 v[46:47], v[46:47], v[126:127] op_sel_hi:[1,0]
	v_pk_mul_f32 v[44:45], v[44:45], v[126:127] op_sel_hi:[1,0]
	v_pk_mul_f32 v[42:43], v[42:43], v[126:127] op_sel_hi:[1,0]
	v_pk_mul_f32 v[40:41], v[40:41], v[126:127] op_sel_hi:[1,0]
	s_waitcnt lgkmcnt(0)
	v_mfma_f32_32x32x16_bf16 v[2:17], v[78:81], v[74:77], v[2:17]
	v_mul_f32_e64 v38, v38, v126
	v_mul_f32_e64 v39, v39, v126
	v_mul_f32_e64 v36, v36, v126
	v_mul_f32_e64 v37, v37, v126
	v_mul_f32_e64 v34, v34, v126
	v_mul_f32_e64 v35, v35, v126
	v_pk_mul_f32 v[64:65], v[64:65], v[126:127] op_sel_hi:[1,0]
	v_pk_mul_f32 v[62:63], v[62:63], v[126:127] op_sel_hi:[1,0]
	v_pk_mul_f32 v[60:61], v[60:61], v[126:127] op_sel_hi:[1,0]
	v_pk_mul_f32 v[58:59], v[58:59], v[126:127] op_sel_hi:[1,0]
	v_mfma_f32_32x32x16_bf16 v[2:17], v[122:125], v[114:117], v[2:17]
	ds_read_b128 v[78:81], v177 offset:35840
	ds_read_b128 v[122:125], v177 offset:36864
	v_mul_f32_e64 v56, v56, v126
	v_mul_f32_e64 v57, v57, v126
	v_mul_f32_e64 v54, v54, v126
	v_mul_f32_e64 v55, v55, v126
	v_pk_mul_f32 v[52:53], v[52:53], v[126:127] op_sel_hi:[1,0]
	v_pk_mul_f32 v[50:51], v[50:51], v[126:127] op_sel_hi:[1,0]
	s_cselect_b32 s64, s64, s65
	s_cmp_gt_i32 s64, 3
	s_waitcnt lgkmcnt(0)
	v_mfma_f32_32x32x16_bf16 v[18:33], v[122:125], v[66:69], v[18:33]
	s_cselect_b64 s[48:49], -1, 0
	s_cmp_lt_i32 s64, 4
	v_mfma_f32_32x32x16_bf16 v[2:17], v[78:81], v[118:121], v[2:17]
	ds_read_b128 v[78:81], v177 offset:37888
	ds_read_b128 v[122:125], v177 offset:38912
	s_waitcnt lgkmcnt(0)
	v_mfma_f32_32x32x16_bf16 v[18:33], v[78:81], v[74:77], v[18:33]
	v_mfma_f32_32x32x16_bf16 v[18:33], v[122:125], v[114:117], v[18:33]
	ds_read_b128 v[78:81], v177 offset:39936
	ds_read_b128 v[122:125], v177 offset:40960
	s_waitcnt lgkmcnt(0)
	v_mfma_f32_32x32x16_bf16 v[34:49], v[122:125], v[66:69], v[34:49]
	v_mfma_f32_32x32x16_bf16 v[18:33], v[78:81], v[118:121], v[18:33]
	ds_read_b128 v[78:81], v177 offset:41984
	ds_read_b128 v[122:125], v177 offset:43008
	s_waitcnt lgkmcnt(0)
	v_mfma_f32_32x32x16_bf16 v[34:49], v[78:81], v[74:77], v[34:49]
	v_mfma_f32_32x32x16_bf16 v[34:49], v[122:125], v[114:117], v[34:49]
	ds_read_b128 v[78:81], v177 offset:44032
	ds_read_b128 v[122:125], v177 offset:45056
	s_waitcnt lgkmcnt(0)
	v_mfma_f32_32x32x16_bf16 v[50:65], v[122:125], v[66:69], v[50:65]
	v_mfma_f32_32x32x16_bf16 v[34:49], v[78:81], v[118:121], v[34:49]
	ds_read_b128 v[66:69], v177 offset:46080
	ds_read_b128 v[78:81], v177 offset:47104
	s_waitcnt lgkmcnt(0)
	v_mfma_f32_32x32x16_bf16 v[50:65], v[66:69], v[74:77], v[50:65]
	v_mfma_f32_32x32x16_bf16 v[50:65], v[78:81], v[114:117], v[50:65]
	v_mfma_f32_32x32x16_bf16 v[82:97], v[130:133], v[118:121], v[82:97]
	v_mfma_f32_32x32x16_bf16 v[50:65], v[70:73], v[118:121], v[50:65]
	s_cbranch_scc1 .LBB0_630
; __device__ __forceinline__ bf16_t f2bf(float a) { return (bf16_t)(pk(a, 0.f) & 0xffffu); }
; __device__ __forceinline__ void p4_scan(Frame& F) {
;     ...
;         const int cidx = STEP_CIDX(n);
;         stored = cidx >= CTXL / 64;
;         if (cidx >= CTXL / 64) { const int rowbase = b * SEQ + (cidx - CTXL / 64) * 64;
; #pragma unroll
;             for (int mt = 0; mt < 2; ++mt)
; #pragma unroll
;                 for (int reg = 0; reg < 16; ++reg) { const int row = 32 * mt + (reg & 3) + 8 * (reg >> 2) + 4 * hh, prow = rowbase + (dir ? 63 - row : row);
;                     OGb[(size_t)prow * 1024 + h * 128 + 32 * nt + c] = f2bf(O[mt][reg]); } }
	s_lshl_b32 s64, s64, 6
	s_add_i32 s64, s61, s64
	v_or_b32_e32 v66, s64, v141
	v_cvt_pk_bf16_f32 v68, v98, s0
	v_lshl_add_u32 v66, v66, 11, v142
	global_store_short v66, v68, s[98:99]
	v_or_b32_e32 v67, s64, v144
	v_cvt_pk_bf16_f32 v69, v99, s0
	v_lshl_add_u32 v67, v67, 11, v142
	global_store_short v67, v69, s[98:99]
	v_or_b32_e32 v66, s64, v145
	v_cvt_pk_bf16_f32 v68, v100, s0
	v_lshl_add_u32 v66, v66, 11, v142
	global_store_short v66, v68, s[98:99]
	v_or_b32_e32 v67, s64, v146
	v_cvt_pk_bf16_f32 v69, v101, s0
	v_lshl_add_u32 v67, v67, 11, v142
	global_store_short v67, v69, s[98:99]
	v_or_b32_e32 v66, s64, v147
	v_cvt_pk_bf16_f32 v68, v102, s0
	v_lshl_add_u32 v66, v66, 11, v142
	global_store_short v66, v68, s[98:99]
	v_or_b32_e32 v67, s64, v148
	v_cvt_pk_bf16_f32 v69, v103, s0
	v_lshl_add_u32 v67, v67, 11, v142
	global_store_short v67, v69, s[98:99]
	v_or_b32_e32 v66, s64, v149
	v_cvt_pk_bf16_f32 v68, v104, s0
	v_lshl_add_u32 v66, v66, 11, v142
	global_store_short v66, v68, s[98:99]
	v_or_b32_e32 v67, s64, v150
	v_cvt_pk_bf16_f32 v69, v105, s0
	v_lshl_add_u32 v67, v67, 11, v142
	global_store_short v67, v69, s[98:99]
	v_or_b32_e32 v66, s64, v151
	v_cvt_pk_bf16_f32 v68, v106, s0
	v_lshl_add_u32 v66, v66, 11, v142
	global_store_short v66, v68, s[98:99]
	v_or_b32_e32 v67, s64, v152
	v_cvt_pk_bf16_f32 v69, v107, s0
	v_lshl_add_u32 v67, v67, 11, v142
	global_store_short v67, v69, s[98:99]
	v_or_b32_e32 v66, s64, v153
	v_cvt_pk_bf16_f32 v68, v108, s0
	v_lshl_add_u32 v66, v66, 11, v142
	global_store_short v66, v68, s[98:99]
	v_or_b32_e32 v67, s64, v154
	v_cvt_pk_bf16_f32 v69, v109, s0
	v_lshl_add_u32 v67, v67, 11, v142
	global_store_short v67, v69, s[98:99]
	v_or_b32_e32 v66, s64, v155
	v_cvt_pk_bf16_f32 v68, v110, s0
	v_lshl_add_u32 v66, v66, 11, v142
	global_store_short v66, v68, s[98:99]
	v_or_b32_e32 v67, s64, v156
	v_cvt_pk_bf16_f32 v69, v111, s0
	v_lshl_add_u32 v67, v67, 11, v142
	global_store_short v67, v69, s[98:99]
	v_or_b32_e32 v66, s64, v157
	v_cvt_pk_bf16_f32 v68, v112, s0
	v_lshl_add_u32 v66, v66, 11, v142
	global_store_short v66, v68, s[98:99]
	v_or_b32_e32 v67, s64, v158
	v_cvt_pk_bf16_f32 v69, v113, s0
	v_lshl_add_u32 v67, v67, 11, v142
	global_store_short v67, v69, s[98:99]
	v_or_b32_e32 v66, s64, v159
	v_cvt_pk_bf16_f32 v68, v82, s0
	v_lshl_add_u32 v66, v66, 11, v142
	global_store_short v66, v68, s[98:99]
	v_or_b32_e32 v67, s64, v160
	v_cvt_pk_bf16_f32 v69, v83, s0
	v_lshl_add_u32 v67, v67, 11, v142
	global_store_short v67, v69, s[98:99]
	v_or_b32_e32 v66, s64, v161
	v_cvt_pk_bf16_f32 v68, v84, s0
	v_lshl_add_u32 v66, v66, 11, v142
	global_store_short v66, v68, s[98:99]
	v_or_b32_e32 v67, s64, v163
	v_cvt_pk_bf16_f32 v69, v85, s0
	v_lshl_add_u32 v67, v67, 11, v142
	global_store_short v67, v69, s[98:99]
	v_or_b32_e32 v66, s64, v164
	v_cvt_pk_bf16_f32 v68, v86, s0
	v_lshl_add_u32 v66, v66, 11, v142
	global_store_short v66, v68, s[98:99]
	v_or_b32_e32 v67, s64, v165
	v_cvt_pk_bf16_f32 v69, v87, s0
	v_lshl_add_u32 v67, v67, 11, v142
	global_store_short v67, v69, s[98:99]
	v_or_b32_e32 v66, s64, v166
	v_cvt_pk_bf16_f32 v68, v88, s0
	v_lshl_add_u32 v66, v66, 11, v142
	global_store_short v66, v68, s[98:99]
	v_or_b32_e32 v67, s64, v167
	v_cvt_pk_bf16_f32 v69, v89, s0
	v_lshl_add_u32 v67, v67, 11, v142
	global_store_short v67, v69, s[98:99]
	v_or_b32_e32 v66, s64, v168
	v_cvt_pk_bf16_f32 v68, v90, s0
	v_lshl_add_u32 v66, v66, 11, v142
	global_store_short v66, v68, s[98:99]
	v_or_b32_e32 v67, s64, v169
	v_cvt_pk_bf16_f32 v69, v91, s0
	v_lshl_add_u32 v67, v67, 11, v142
	global_store_short v67, v69, s[98:99]
	v_or_b32_e32 v66, s64, v170
	v_cvt_pk_bf16_f32 v68, v92, s0
	v_lshl_add_u32 v66, v66, 11, v142
	global_store_short v66, v68, s[98:99]
	v_or_b32_e32 v67, s64, v171
	v_cvt_pk_bf16_f32 v69, v93, s0
	v_lshl_add_u32 v67, v67, 11, v142
	global_store_short v67, v69, s[98:99]
	v_or_b32_e32 v66, s64, v172
	v_cvt_pk_bf16_f32 v68, v94, s0
	v_lshl_add_u32 v66, v66, 11, v142
	global_store_short v66, v68, s[98:99]
	v_or_b32_e32 v67, s64, v173
	v_cvt_pk_bf16_f32 v69, v95, s0
	v_lshl_add_u32 v67, v67, 11, v142
	global_store_short v67, v69, s[98:99]
	v_or_b32_e32 v66, s64, v174
	v_cvt_pk_bf16_f32 v68, v96, s0
	v_lshl_add_u32 v66, v66, 11, v142
	global_store_short v66, v68, s[98:99]
	v_or_b32_e32 v67, s64, v175
	v_cvt_pk_bf16_f32 v69, v97, s0
	v_lshl_add_u32 v67, v67, 11, v142
	global_store_short v67, v69, s[98:99]
	s_branch .LBB0_630
